# plus non-temporal stores for the converted fp8 expert weights written during the attention phase
# speedup vs baseline: 1.0112x; 1.0112x over previous
; #define LAS __attribute__((address_space(3)))
; template <bool F8> DI void item_gather(const TItem& d, LAS float* scr, int lane) {
;     if constexpr (F8) {
;         const int nl = lane >> 2, kc = lane & 3;
;         unsigned char* base = d.WT + (size_t)d.drow0 * d.Kd + d.kofs + d.k0;
;         unsigned voff = (unsigned)(nl * d.Kd + 16 * kc); asm volatile("" : "+v"(voff));
;         f32x4 x[16];
; #pragma unroll
;         for (int t = 0; t < 4; ++t) { const int n = nl + 16 * t; const int sw = 4 * (((n >> 2) & 15) ^ (n & 3));
; #pragma unroll
;             for (int q = 0; q < 4; ++q) { const int kq = 16 * kc + 4 * q; x[t * 4 + q] = *(const LAS f32x4*)(scr + n * 64 + (kq ^ sw)); } }
;         asm volatile("s_waitcnt lgkmcnt(0)" : "+v"(x[0]), "+v"(x[1]), "+v"(x[2]), "+v"(x[3]), "+v"(x[4]), "+v"(x[5]), "+v"(x[6]), "+v"(x[7]),
;                      "+v"(x[8]), "+v"(x[9]), "+v"(x[10]), "+v"(x[11]), "+v"(x[12]), "+v"(x[13]), "+v"(x[14]), "+v"(x[15]) :: "memory");
.LBB0_469:
	v_mad_u64_u32 v[198:199], s[18:19], s8, v175, v[90:91]
	ds_read_b128 v[66:69], v192
	ds_read_b128 v[70:73], v191
	ds_read_b128 v[74:77], v190
	ds_read_b128 v[78:81], v189
	ds_read_b128 v[82:85], v188
	ds_read_b128 v[86:89], v187
	ds_read_b128 v[214:217], v185
	ds_read_b128 v[218:221], v184
	ds_read_b128 v[222:225], v183
	ds_read_b128 v[226:229], v182
	ds_read_b128 v[230:233], v181
	ds_read_b128 v[234:237], v180
	ds_read_b128 v[238:241], v179
	ds_read_b128 v[242:245], v178
	ds_read_b128 v[246:249], v177
	ds_read_b128 v[194:197], v176
	s_add_u32 s10, s10, s42
	s_addc_u32 s11, s11, s37
	s_waitcnt lgkmcnt(0)
	s_waitcnt lgkmcnt(0)
; DI unsigned pk4_fp8(float a, float b, float c, float d) { int r = 0; r = __builtin_amdgcn_cvt_pk_fp8_f32(sat8(a), sat8(b), r, false); r = __builtin_amdgcn_cvt_pk_fp8_f32(sat8(c), sat8(d), r, true); return (unsigned)r; }
; DI float sat8(float x) { return __builtin_amdgcn_fmed3f(x, -448.0f, 448.0f); }
; template <bool F8> DI void item_gather(const TItem& d, LAS float* scr, int lane) {
;     ...
;         for (int t = 0; t < 4; ++t) { u32x4 o;
; #pragma unroll
;             for (int q = 0; q < 4; ++q) { const f32x4 y = x[t * 4 + q]; o[q] = pk4_fp8(y[0] * W8_SCALE, y[1] * W8_SCALE, y[2] * W8_SCALE, y[3] * W8_SCALE); }
;             *(u32x4*)(base + (size_t)t * 16 * d.Kd + voff) = o; }
	s_nop 0
	v_mul_f32_e32 v0, 0x42800000, v194
	v_mul_f32_e32 v193, 0x42800000, v195
	v_med3_f32 v0, v0, s53, v204
	v_med3_f32 v193, v193, s53, v204
	v_mov_b32_e32 v194, v1
	v_cvt_pk_fp8_f32 v194, v0, v193
	v_mul_f32_e32 v195, 0x42800000, v196
	v_mul_f32_e32 v196, 0x42800000, v197
	v_med3_f32 v0, v195, s53, v204
	v_med3_f32 v193, v196, s53, v204
	v_cvt_pk_fp8_f32 v194, v0, v193 op_sel:[0,0,1]
	v_mul_f32_e32 v0, 0x42800000, v246
	v_mul_f32_e32 v193, 0x42800000, v247
	v_med3_f32 v0, v0, s53, v204
	v_med3_f32 v193, v193, s53, v204
	v_mov_b32_e32 v195, v1
	v_cvt_pk_fp8_f32 v195, v0, v193
	v_mul_f32_e32 v196, 0x42800000, v248
	v_mul_f32_e32 v197, 0x42800000, v249
	v_med3_f32 v0, v196, s53, v204
	v_med3_f32 v193, v197, s53, v204
	s_add_u32 s10, s10, s33
	v_cvt_pk_fp8_f32 v195, v0, v193 op_sel:[0,0,1]
	v_mul_f32_e32 v0, 0x42800000, v242
	v_mul_f32_e32 v193, 0x42800000, v243
	s_addc_u32 s11, s11, s41
	v_med3_f32 v0, v0, s53, v204
	v_med3_f32 v193, v193, s53, v204
	v_mov_b32_e32 v196, v1
	s_add_u32 s10, s10, s39
	v_cvt_pk_fp8_f32 v196, v0, v193
	s_addc_u32 s11, s11, s36
	v_mov_b32_e32 v199, v1
	v_lshl_add_u64 v[200:201], s[10:11], 0, v[198:199]
	v_mul_f32_e32 v197, 0x42800000, v244
	v_mul_f32_e32 v199, 0x42800000, v245
	v_med3_f32 v0, v197, s53, v204
	v_med3_f32 v193, v199, s53, v204
	v_cvt_pk_fp8_f32 v196, v0, v193 op_sel:[0,0,1]
	v_mul_f32_e32 v0, 0x42800000, v238
	v_mul_f32_e32 v193, 0x42800000, v239
	v_med3_f32 v0, v0, s53, v204
	v_med3_f32 v193, v193, s53, v204
	v_mov_b32_e32 v197, v1
	v_cvt_pk_fp8_f32 v197, v0, v193
	v_mul_f32_e32 v199, 0x42800000, v240
	v_mul_f32_e32 v202, 0x42800000, v241
	v_med3_f32 v0, v199, s53, v204
	v_med3_f32 v193, v202, s53, v204
	v_cvt_pk_fp8_f32 v197, v0, v193 op_sel:[0,0,1]
	v_mul_f32_e32 v0, 0x42800000, v234
	v_mul_f32_e32 v193, 0x42800000, v235
	v_med3_f32 v0, v0, s53, v204
	global_store_dwordx4 v198, v[194:197], s[10:11] nt
	v_med3_f32 v193, v193, s53, v204
	v_mul_f32_e32 v198, 0x42800000, v229
	v_mov_b32_e32 v194, v1
	v_cvt_pk_fp8_f32 v194, v0, v193
	v_mul_f32_e32 v195, 0x42800000, v236
	v_mul_f32_e32 v196, 0x42800000, v237
	v_med3_f32 v0, v195, s53, v204
	v_med3_f32 v193, v196, s53, v204
	v_cvt_pk_fp8_f32 v194, v0, v193 op_sel:[0,0,1]
	v_mul_f32_e32 v0, 0x42800000, v230
	v_mul_f32_e32 v193, 0x42800000, v231
	v_med3_f32 v0, v0, s53, v204
	v_med3_f32 v193, v193, s53, v204
	v_mov_b32_e32 v195, v1
	v_cvt_pk_fp8_f32 v195, v0, v193
	v_mul_f32_e32 v196, 0x42800000, v232
	v_mul_f32_e32 v197, 0x42800000, v233
	v_med3_f32 v0, v196, s53, v204
	v_med3_f32 v193, v197, s53, v204
	v_cvt_pk_fp8_f32 v195, v0, v193 op_sel:[0,0,1]
	v_mul_f32_e32 v0, 0x42800000, v226
	v_mul_f32_e32 v193, 0x42800000, v227
	v_med3_f32 v0, v0, s53, v204
	v_med3_f32 v193, v193, s53, v204
	v_mov_b32_e32 v196, v1
	v_cvt_pk_fp8_f32 v196, v0, v193
	v_mul_f32_e32 v197, 0x42800000, v228
	v_med3_f32 v0, v197, s53, v204
	v_med3_f32 v193, v198, s53, v204
	v_cvt_pk_fp8_f32 v196, v0, v193 op_sel:[0,0,1]
	v_mul_f32_e32 v0, 0x42800000, v222
	v_mul_f32_e32 v193, 0x42800000, v223
	v_med3_f32 v0, v0, s53, v204
	v_med3_f32 v193, v193, s53, v204
	v_mov_b32_e32 v197, v1
	v_cvt_pk_fp8_f32 v197, v0, v193
	v_mul_f32_e32 v198, 0x42800000, v224
	v_mul_f32_e32 v199, 0x42800000, v225
	v_med3_f32 v0, v198, s53, v204
	v_med3_f32 v193, v199, s53, v204
	v_cvt_pk_fp8_f32 v197, v0, v193 op_sel:[0,0,1]
	s_lshl_b64 s[8:9], s[8:9], 4
	v_lshl_add_u64 v[198:199], v[200:201], 0, s[8:9]
	v_mul_f32_e32 v0, 0x42800000, v218
	v_mul_f32_e32 v193, 0x42800000, v219
	global_store_dwordx4 v[198:199], v[194:197], off nt
	v_med3_f32 v0, v0, s53, v204
	v_med3_f32 v193, v193, s53, v204
	v_mov_b32_e32 v194, v1
	v_cvt_pk_fp8_f32 v194, v0, v193
	v_mul_f32_e32 v195, 0x42800000, v220
	v_mul_f32_e32 v196, 0x42800000, v221
	v_med3_f32 v0, v195, s53, v204
	v_med3_f32 v193, v196, s53, v204
	v_cvt_pk_fp8_f32 v194, v0, v193 op_sel:[0,0,1]
	v_mul_f32_e32 v0, 0x42800000, v214
	v_mul_f32_e32 v193, 0x42800000, v215
	v_med3_f32 v0, v0, s53, v204
	v_med3_f32 v193, v193, s53, v204
	v_mov_b32_e32 v195, v1
	v_cvt_pk_fp8_f32 v195, v0, v193
	v_mul_f32_e32 v196, 0x42800000, v216
	v_mul_f32_e32 v197, 0x42800000, v217
	v_med3_f32 v0, v196, s53, v204
	v_med3_f32 v193, v197, s53, v204
	v_cvt_pk_fp8_f32 v195, v0, v193 op_sel:[0,0,1]
	v_mul_f32_e32 v0, 0x42800000, v86
	v_mul_f32_e32 v86, 0x42800000, v87
	v_med3_f32 v0, v0, s53, v204
	v_med3_f32 v86, v86, s53, v204
	v_mov_b32_e32 v196, v1
	v_cvt_pk_fp8_f32 v196, v0, v86
	v_mul_f32_e32 v87, 0x42800000, v88
	v_mul_f32_e32 v88, 0x42800000, v89
	v_med3_f32 v0, v87, s53, v204
	v_med3_f32 v86, v88, s53, v204
	v_cvt_pk_fp8_f32 v196, v0, v86 op_sel:[0,0,1]
	v_mul_f32_e32 v0, 0x42800000, v82
	v_mul_f32_e32 v82, 0x42800000, v83
	v_med3_f32 v0, v0, s53, v204
	v_med3_f32 v82, v82, s53, v204
	v_mov_b32_e32 v197, v1
	v_cvt_pk_fp8_f32 v197, v0, v82
	v_mul_f32_e32 v83, 0x42800000, v84
	v_mul_f32_e32 v84, 0x42800000, v85
	v_med3_f32 v0, v83, s53, v204
	v_med3_f32 v82, v84, s53, v204
	v_cvt_pk_fp8_f32 v197, v0, v82 op_sel:[0,0,1]
	v_mul_f32_e32 v0, 0x42800000, v78
	v_mul_f32_e32 v78, 0x42800000, v79
	v_mul_f32_e32 v79, 0x42800000, v80
	v_mul_f32_e32 v80, 0x42800000, v81
	v_med3_f32 v0, v0, s53, v204
	v_med3_f32 v81, v78, s53, v204
	v_mov_b32_e32 v78, v1
	v_cvt_pk_fp8_f32 v78, v0, v81
	v_med3_f32 v0, v79, s53, v204
	v_med3_f32 v79, v80, s53, v204
	v_mov_b32_e32 v80, v1
	v_cvt_pk_fp8_f32 v78, v0, v79 op_sel:[0,0,1]
	v_mul_f32_e32 v0, 0x42800000, v74
	v_mul_f32_e32 v74, 0x42800000, v75
	v_med3_f32 v0, v0, s53, v204
	v_med3_f32 v74, v74, s53, v204
	v_mov_b32_e32 v79, v1
	v_cvt_pk_fp8_f32 v79, v0, v74
	v_mul_f32_e32 v75, 0x42800000, v76
	v_mul_f32_e32 v76, 0x42800000, v77
	v_med3_f32 v0, v75, s53, v204
	v_med3_f32 v74, v76, s53, v204
	v_cvt_pk_fp8_f32 v79, v0, v74 op_sel:[0,0,1]
	v_mul_f32_e32 v0, 0x42800000, v70
	v_mul_f32_e32 v70, 0x42800000, v71
	v_med3_f32 v0, v0, s53, v204
	v_med3_f32 v70, v70, s53, v204
	v_cvt_pk_fp8_f32 v80, v0, v70
	v_mul_f32_e32 v71, 0x42800000, v72
	v_mul_f32_e32 v72, 0x42800000, v73
	v_med3_f32 v0, v71, s53, v204
	v_med3_f32 v70, v72, s53, v204
	v_cvt_pk_fp8_f32 v80, v0, v70 op_sel:[0,0,1]
	v_mul_f32_e32 v0, 0x42800000, v66
	v_mul_f32_e32 v66, 0x42800000, v67
	v_med3_f32 v0, v0, s53, v204
	v_med3_f32 v66, v66, s53, v204
	v_mov_b32_e32 v81, v1
	v_cvt_pk_fp8_f32 v81, v0, v66
	v_mul_f32_e32 v67, 0x42800000, v68
	v_mul_f32_e32 v68, 0x42800000, v69
	v_med3_f32 v0, v67, s53, v204
	v_med3_f32 v66, v68, s53, v204
	v_cvt_pk_fp8_f32 v81, v0, v66 op_sel:[0,0,1]
	v_lshl_add_u64 v[82:83], v[198:199], 0, s[8:9]
	v_lshl_add_u64 v[66:67], v[82:83], 0, s[8:9]
	global_store_dwordx4 v[82:83], v[194:197], off nt
	global_store_dwordx4 v[66:67], v[78:81], off nt
	s_waitcnt lgkmcnt(0)
	s_andn2_b64 vcc, exec, s[2:3]
	s_add_i32 s38, s38, 1
	s_cbranch_vccz .LBB0_472

; #define LAS __attribute__((address_space(3)))
; template <bool F8> DI void item_gather(const TItem& d, LAS float* scr, int lane) {
;     if constexpr (F8) {
;         const int nl = lane >> 2, kc = lane & 3;
;         unsigned char* base = d.WT + (size_t)d.drow0 * d.Kd + d.kofs + d.k0;
;         unsigned voff = (unsigned)(nl * d.Kd + 16 * kc); asm volatile("" : "+v"(voff));
;         f32x4 x[16];
; #pragma unroll
;         for (int t = 0; t < 4; ++t) { const int n = nl + 16 * t; const int sw = 4 * (((n >> 2) & 15) ^ (n & 3));
; #pragma unroll
;             for (int q = 0; q < 4; ++q) { const int kq = 16 * kc + 4 * q; x[t * 4 + q] = *(const LAS f32x4*)(scr + n * 64 + (kq ^ sw)); } }
;         asm volatile("s_waitcnt lgkmcnt(0)" : "+v"(x[0]), "+v"(x[1]), "+v"(x[2]), "+v"(x[3]), "+v"(x[4]), "+v"(x[5]), "+v"(x[6]), "+v"(x[7]),
;                      "+v"(x[8]), "+v"(x[9]), "+v"(x[10]), "+v"(x[11]), "+v"(x[12]), "+v"(x[13]), "+v"(x[14]), "+v"(x[15]) :: "memory");
.LBB0_641:
	v_mad_u64_u32 v[198:199], s[18:19], s8, v175, v[90:91]
	ds_read_b128 v[66:69], v192
	ds_read_b128 v[70:73], v191
	ds_read_b128 v[74:77], v190
	ds_read_b128 v[78:81], v189
	ds_read_b128 v[82:85], v188
	ds_read_b128 v[86:89], v187
	ds_read_b128 v[194:197], v185
	ds_read_b128 v[214:217], v184
	ds_read_b128 v[218:221], v183
	ds_read_b128 v[222:225], v182
	ds_read_b128 v[226:229], v181
	ds_read_b128 v[230:233], v180
	ds_read_b128 v[234:237], v179
	ds_read_b128 v[238:241], v178
	ds_read_b128 v[242:245], v177
	ds_read_b128 v[246:249], v176
	s_add_u32 s10, s10, s48
	s_addc_u32 s11, s11, s42
	s_add_u32 s10, s10, s33
	s_waitcnt lgkmcnt(0)
	s_waitcnt lgkmcnt(0)
; DI unsigned pk4_fp8(float a, float b, float c, float d) { int r = 0; r = __builtin_amdgcn_cvt_pk_fp8_f32(sat8(a), sat8(b), r, false); r = __builtin_amdgcn_cvt_pk_fp8_f32(sat8(c), sat8(d), r, true); return (unsigned)r; }
; DI float sat8(float x) { return __builtin_amdgcn_fmed3f(x, -448.0f, 448.0f); }
; template <bool F8> DI void item_gather(const TItem& d, LAS float* scr, int lane) {
;     ...
;         for (int t = 0; t < 4; ++t) { u32x4 o;
; #pragma unroll
;             for (int q = 0; q < 4; ++q) { const f32x4 y = x[t * 4 + q]; o[q] = pk4_fp8(y[0] * W8_SCALE, y[1] * W8_SCALE, y[2] * W8_SCALE, y[3] * W8_SCALE); }
;             *(u32x4*)(base + (size_t)t * 16 * d.Kd + voff) = o; }
	s_nop 0
	v_mul_f32_e32 v0, 0x42800000, v246
	v_mul_f32_e32 v193, 0x42800000, v247
	s_addc_u32 s11, s11, s43
	v_med3_f32 v0, v0, s53, v204
	v_med3_f32 v193, v193, s53, v204
	v_mov_b32_e32 v246, v1
	s_add_u32 s10, s10, s39
	v_cvt_pk_fp8_f32 v246, v0, v193
	s_addc_u32 s11, s11, s41
	v_mov_b32_e32 v199, v1
	v_lshl_add_u64 v[200:201], s[10:11], 0, v[198:199]
	v_mul_f32_e32 v199, 0x42800000, v248
	v_mul_f32_e32 v202, 0x42800000, v249
	v_med3_f32 v0, v199, s53, v204
	v_med3_f32 v193, v202, s53, v204
	v_cvt_pk_fp8_f32 v246, v0, v193 op_sel:[0,0,1]
	v_mul_f32_e32 v0, 0x42800000, v242
	v_mul_f32_e32 v193, 0x42800000, v243
	v_med3_f32 v0, v0, s53, v204
	v_med3_f32 v193, v193, s53, v204
	v_mov_b32_e32 v247, v1
	v_cvt_pk_fp8_f32 v247, v0, v193
	v_mul_f32_e32 v199, 0x42800000, v244
	v_mul_f32_e32 v202, 0x42800000, v245
	v_med3_f32 v0, v199, s53, v204
	v_med3_f32 v193, v202, s53, v204
	v_cvt_pk_fp8_f32 v247, v0, v193 op_sel:[0,0,1]
	v_mul_f32_e32 v0, 0x42800000, v238
	v_mul_f32_e32 v193, 0x42800000, v239
	v_med3_f32 v0, v0, s53, v204
	v_med3_f32 v193, v193, s53, v204
	v_mov_b32_e32 v248, v1
	v_cvt_pk_fp8_f32 v248, v0, v193
	v_mul_f32_e32 v199, 0x42800000, v240
	v_mul_f32_e32 v202, 0x42800000, v241
	v_med3_f32 v0, v199, s53, v204
	v_med3_f32 v193, v202, s53, v204
	v_cvt_pk_fp8_f32 v248, v0, v193 op_sel:[0,0,1]
	v_mul_f32_e32 v0, 0x42800000, v234
	v_mul_f32_e32 v193, 0x42800000, v235
	v_med3_f32 v0, v0, s53, v204
	v_med3_f32 v193, v193, s53, v204
	v_mov_b32_e32 v249, v1
	v_cvt_pk_fp8_f32 v249, v0, v193
	v_mul_f32_e32 v199, 0x42800000, v236
	v_mul_f32_e32 v202, 0x42800000, v237
	v_med3_f32 v0, v199, s53, v204
	v_med3_f32 v193, v202, s53, v204
	v_cvt_pk_fp8_f32 v249, v0, v193 op_sel:[0,0,1]
	v_mul_f32_e32 v0, 0x42800000, v230
	v_mul_f32_e32 v193, 0x42800000, v231
	v_med3_f32 v0, v0, s53, v204
	v_med3_f32 v193, v193, s53, v204
	v_mov_b32_e32 v230, v1
	v_cvt_pk_fp8_f32 v230, v0, v193
	global_store_dwordx4 v198, v[246:249], s[10:11] nt
	v_mul_f32_e32 v198, 0x42800000, v232
	v_mul_f32_e32 v199, 0x42800000, v233
	v_med3_f32 v0, v198, s53, v204
	v_med3_f32 v193, v199, s53, v204
	v_cvt_pk_fp8_f32 v230, v0, v193 op_sel:[0,0,1]
	v_mul_f32_e32 v0, 0x42800000, v226
	v_mul_f32_e32 v193, 0x42800000, v227
	v_med3_f32 v0, v0, s53, v204
	v_med3_f32 v193, v193, s53, v204
	v_mov_b32_e32 v231, v1
	v_cvt_pk_fp8_f32 v231, v0, v193
	v_mul_f32_e32 v198, 0x42800000, v228
	v_mul_f32_e32 v199, 0x42800000, v229
	v_med3_f32 v0, v198, s53, v204
	v_med3_f32 v193, v199, s53, v204
	v_cvt_pk_fp8_f32 v231, v0, v193 op_sel:[0,0,1]
	v_mul_f32_e32 v0, 0x42800000, v222
	v_mul_f32_e32 v193, 0x42800000, v223
	v_med3_f32 v0, v0, s53, v204
	v_med3_f32 v193, v193, s53, v204
	v_mov_b32_e32 v232, v1
	v_cvt_pk_fp8_f32 v232, v0, v193
	v_mul_f32_e32 v198, 0x42800000, v224
	v_mul_f32_e32 v199, 0x42800000, v225
	v_med3_f32 v0, v198, s53, v204
	v_med3_f32 v193, v199, s53, v204
	v_cvt_pk_fp8_f32 v232, v0, v193 op_sel:[0,0,1]
	v_mul_f32_e32 v0, 0x42800000, v218
	v_mul_f32_e32 v193, 0x42800000, v219
	v_med3_f32 v0, v0, s53, v204
	v_med3_f32 v193, v193, s53, v204
	v_mov_b32_e32 v233, v1
	v_cvt_pk_fp8_f32 v233, v0, v193
	v_mul_f32_e32 v198, 0x42800000, v220
	v_mul_f32_e32 v199, 0x42800000, v221
	v_med3_f32 v0, v198, s53, v204
	v_med3_f32 v193, v199, s53, v204
	v_cvt_pk_fp8_f32 v233, v0, v193 op_sel:[0,0,1]
	v_mul_f32_e32 v0, 0x42800000, v214
	v_mul_f32_e32 v193, 0x42800000, v215
	v_med3_f32 v0, v0, s53, v204
	v_med3_f32 v193, v193, s53, v204
	v_mov_b32_e32 v214, v1
	v_cvt_pk_fp8_f32 v214, v0, v193
	s_lshl_b64 s[8:9], s[8:9], 4
	v_lshl_add_u64 v[198:199], v[200:201], 0, s[8:9]
	v_mul_f32_e32 v200, 0x42800000, v216
	v_mul_f32_e32 v201, 0x42800000, v217
	v_med3_f32 v0, v200, s53, v204
	v_med3_f32 v193, v201, s53, v204
	v_cvt_pk_fp8_f32 v214, v0, v193 op_sel:[0,0,1]
	v_mul_f32_e32 v0, 0x42800000, v194
	v_mul_f32_e32 v193, 0x42800000, v195
	v_med3_f32 v0, v0, s53, v204
	v_med3_f32 v193, v193, s53, v204
	v_mov_b32_e32 v215, v1
	v_cvt_pk_fp8_f32 v215, v0, v193
	v_mul_f32_e32 v194, 0x42800000, v196
	v_mul_f32_e32 v195, 0x42800000, v197
	v_med3_f32 v0, v194, s53, v204
	v_med3_f32 v193, v195, s53, v204
	v_cvt_pk_fp8_f32 v215, v0, v193 op_sel:[0,0,1]
	v_mul_f32_e32 v0, 0x42800000, v86
	v_mul_f32_e32 v86, 0x42800000, v87
	v_med3_f32 v0, v0, s53, v204
	v_med3_f32 v86, v86, s53, v204
	v_mov_b32_e32 v216, v1
	v_cvt_pk_fp8_f32 v216, v0, v86
	v_mul_f32_e32 v87, 0x42800000, v88
	v_mul_f32_e32 v88, 0x42800000, v89
	v_med3_f32 v0, v87, s53, v204
	v_med3_f32 v86, v88, s53, v204
	v_cvt_pk_fp8_f32 v216, v0, v86 op_sel:[0,0,1]
	v_mul_f32_e32 v0, 0x42800000, v82
	v_mul_f32_e32 v82, 0x42800000, v83
	v_med3_f32 v0, v0, s53, v204
	v_med3_f32 v82, v82, s53, v204
	v_mov_b32_e32 v217, v1
	v_cvt_pk_fp8_f32 v217, v0, v82
	v_mul_f32_e32 v83, 0x42800000, v84
	v_mul_f32_e32 v84, 0x42800000, v85
	v_med3_f32 v0, v83, s53, v204
	v_med3_f32 v82, v84, s53, v204
	v_cvt_pk_fp8_f32 v217, v0, v82 op_sel:[0,0,1]
	v_mul_f32_e32 v0, 0x42800000, v78
	v_mul_f32_e32 v78, 0x42800000, v79
	v_mul_f32_e32 v79, 0x42800000, v80
	v_mul_f32_e32 v80, 0x42800000, v81
	v_med3_f32 v0, v0, s53, v204
	v_med3_f32 v81, v78, s53, v204
	v_mov_b32_e32 v78, v1
	v_cvt_pk_fp8_f32 v78, v0, v81
	v_med3_f32 v0, v79, s53, v204
	v_med3_f32 v79, v80, s53, v204
	v_mov_b32_e32 v80, v1
	v_cvt_pk_fp8_f32 v78, v0, v79 op_sel:[0,0,1]
	v_mul_f32_e32 v0, 0x42800000, v74
	v_mul_f32_e32 v74, 0x42800000, v75
	v_med3_f32 v0, v0, s53, v204
	v_med3_f32 v74, v74, s53, v204
	v_mov_b32_e32 v79, v1
	v_cvt_pk_fp8_f32 v79, v0, v74
	v_mul_f32_e32 v75, 0x42800000, v76
	v_mul_f32_e32 v76, 0x42800000, v77
	v_med3_f32 v0, v75, s53, v204
	v_med3_f32 v74, v76, s53, v204
	v_cvt_pk_fp8_f32 v79, v0, v74 op_sel:[0,0,1]
	v_mul_f32_e32 v0, 0x42800000, v70
	v_mul_f32_e32 v70, 0x42800000, v71
	v_med3_f32 v0, v0, s53, v204
	v_med3_f32 v70, v70, s53, v204
	v_cvt_pk_fp8_f32 v80, v0, v70
	v_mul_f32_e32 v71, 0x42800000, v72
	v_mul_f32_e32 v72, 0x42800000, v73
	v_med3_f32 v0, v71, s53, v204
	v_med3_f32 v70, v72, s53, v204
	v_cvt_pk_fp8_f32 v80, v0, v70 op_sel:[0,0,1]
	v_mul_f32_e32 v0, 0x42800000, v66
	v_mul_f32_e32 v66, 0x42800000, v67
	v_med3_f32 v0, v0, s53, v204
	v_med3_f32 v66, v66, s53, v204
	v_mov_b32_e32 v81, v1
	v_cvt_pk_fp8_f32 v81, v0, v66
	v_mul_f32_e32 v67, 0x42800000, v68
	v_mul_f32_e32 v68, 0x42800000, v69
	v_med3_f32 v0, v67, s53, v204
	v_med3_f32 v66, v68, s53, v204
	v_cvt_pk_fp8_f32 v81, v0, v66 op_sel:[0,0,1]
	v_lshl_add_u64 v[82:83], v[198:199], 0, s[8:9]
	v_lshl_add_u64 v[66:67], v[82:83], 0, s[8:9]
	global_store_dwordx4 v[198:199], v[230:233], off nt
	global_store_dwordx4 v[82:83], v[214:217], off nt
	global_store_dwordx4 v[66:67], v[78:81], off nt
	s_waitcnt lgkmcnt(0)
	s_andn2_b64 vcc, exec, s[2:3]
	s_add_i32 s38, s38, 1
	s_cbranch_vccz .LBB0_474

; #define LAS __attribute__((address_space(3)))
; template <bool F8> DI void item_gather(const TItem& d, LAS float* scr, int lane) {
;     if constexpr (F8) {
;         const int nl = lane >> 2, kc = lane & 3;
;         unsigned char* base = d.WT + (size_t)d.drow0 * d.Kd + d.kofs + d.k0;
;         unsigned voff = (unsigned)(nl * d.Kd + 16 * kc); asm volatile("" : "+v"(voff));
;         f32x4 x[16];
; #pragma unroll
;         for (int t = 0; t < 4; ++t) { const int n = nl + 16 * t; const int sw = 4 * (((n >> 2) & 15) ^ (n & 3));
; #pragma unroll
;             for (int q = 0; q < 4; ++q) { const int kq = 16 * kc + 4 * q; x[t * 4 + q] = *(const LAS f32x4*)(scr + n * 64 + (kq ^ sw)); } }
;         asm volatile("s_waitcnt lgkmcnt(0)" : "+v"(x[0]), "+v"(x[1]), "+v"(x[2]), "+v"(x[3]), "+v"(x[4]), "+v"(x[5]), "+v"(x[6]), "+v"(x[7]),
;                      "+v"(x[8]), "+v"(x[9]), "+v"(x[10]), "+v"(x[11]), "+v"(x[12]), "+v"(x[13]), "+v"(x[14]), "+v"(x[15]) :: "memory");
.LBB0_712:
	s_andn2_b64 vcc, exec, s[18:19]
	s_cbranch_vccnz .LBB0_677
	v_mad_u64_u32 v[196:197], s[18:19], s58, v175, v[90:91]
	s_add_u32 s10, s10, s38
	s_addc_u32 s11, s11, s37
	ds_read_b128 v[66:69], v191
	ds_read_b128 v[70:73], v190
	ds_read_b128 v[74:77], v189
	ds_read_b128 v[78:81], v188
	ds_read_b128 v[82:85], v187
	ds_read_b128 v[86:89], v186
	ds_read_b128 v[192:195], v185
	ds_read_b128 v[214:217], v184
	ds_read_b128 v[218:221], v183
	ds_read_b128 v[222:225], v182
	ds_read_b128 v[226:229], v181
	ds_read_b128 v[230:233], v180
	ds_read_b128 v[234:237], v179
	ds_read_b128 v[238:241], v178
	ds_read_b128 v[242:245], v177
	ds_read_b128 v[246:249], v176
	s_add_u32 s10, s10, s30
	s_addc_u32 s11, s11, s31
	s_add_u32 s10, s10, s33
	s_addc_u32 s11, s11, s36
	v_mov_b32_e32 v197, v1
	s_waitcnt lgkmcnt(0)
	s_waitcnt lgkmcnt(0)
; DI unsigned pk4_fp8(float a, float b, float c, float d) { int r = 0; r = __builtin_amdgcn_cvt_pk_fp8_f32(sat8(a), sat8(b), r, false); r = __builtin_amdgcn_cvt_pk_fp8_f32(sat8(c), sat8(d), r, true); return (unsigned)r; }
; DI float sat8(float x) { return __builtin_amdgcn_fmed3f(x, -448.0f, 448.0f); }
; template <bool F8> DI void item_gather(const TItem& d, LAS float* scr, int lane) {
;     ...
;         for (int t = 0; t < 4; ++t) { u32x4 o;
; #pragma unroll
;             for (int q = 0; q < 4; ++q) { const f32x4 y = x[t * 4 + q]; o[q] = pk4_fp8(y[0] * W8_SCALE, y[1] * W8_SCALE, y[2] * W8_SCALE, y[3] * W8_SCALE); }
;             *(u32x4*)(base + (size_t)t * 16 * d.Kd + voff) = o; }
	v_lshl_add_u64 v[198:199], s[10:11], 0, v[196:197]
	v_mul_f32_e32 v0, 0x42800000, v246
	v_mul_f32_e32 v197, 0x42800000, v247
	v_med3_f32 v0, v0, s53, v204
	v_med3_f32 v197, v197, s53, v204
	v_mov_b32_e32 v246, v1
	v_cvt_pk_fp8_f32 v246, v0, v197
	v_mul_f32_e32 v200, 0x42800000, v248
	v_mul_f32_e32 v201, 0x42800000, v249
	v_med3_f32 v0, v200, s53, v204
	v_med3_f32 v197, v201, s53, v204
	v_cvt_pk_fp8_f32 v246, v0, v197 op_sel:[0,0,1]
	v_mul_f32_e32 v0, 0x42800000, v242
	v_mul_f32_e32 v197, 0x42800000, v243
	v_med3_f32 v0, v0, s53, v204
	v_med3_f32 v197, v197, s53, v204
	v_mov_b32_e32 v247, v1
	v_cvt_pk_fp8_f32 v247, v0, v197
	v_mul_f32_e32 v200, 0x42800000, v244
	v_mul_f32_e32 v201, 0x42800000, v245
	v_med3_f32 v0, v200, s53, v204
	v_med3_f32 v197, v201, s53, v204
	v_cvt_pk_fp8_f32 v247, v0, v197 op_sel:[0,0,1]
	v_mul_f32_e32 v0, 0x42800000, v238
	v_mul_f32_e32 v197, 0x42800000, v239
	v_med3_f32 v0, v0, s53, v204
	v_med3_f32 v197, v197, s53, v204
	v_mov_b32_e32 v248, v1
	v_cvt_pk_fp8_f32 v248, v0, v197
	v_mul_f32_e32 v200, 0x42800000, v240
	v_mul_f32_e32 v201, 0x42800000, v241
	v_med3_f32 v0, v200, s53, v204
	v_med3_f32 v197, v201, s53, v204
	v_cvt_pk_fp8_f32 v248, v0, v197 op_sel:[0,0,1]
	v_mul_f32_e32 v0, 0x42800000, v234
	v_mul_f32_e32 v197, 0x42800000, v235
	v_med3_f32 v0, v0, s53, v204
	v_med3_f32 v197, v197, s53, v204
	v_mov_b32_e32 v249, v1
	v_cvt_pk_fp8_f32 v249, v0, v197
	v_mul_f32_e32 v200, 0x42800000, v236
	v_mul_f32_e32 v201, 0x42800000, v237
	v_med3_f32 v0, v200, s53, v204
	v_med3_f32 v197, v201, s53, v204
	v_cvt_pk_fp8_f32 v249, v0, v197 op_sel:[0,0,1]
	v_mul_f32_e32 v0, 0x42800000, v230
	v_med3_f32 v0, v0, s53, v204
	v_mov_b32_e32 v230, v1
	global_store_dwordx4 v196, v[246:249], s[10:11] nt
	v_mul_f32_e32 v196, 0x42800000, v231
	v_med3_f32 v196, v196, s53, v204
	v_cvt_pk_fp8_f32 v230, v0, v196
	v_mul_f32_e32 v197, 0x42800000, v232
	v_mul_f32_e32 v200, 0x42800000, v233
	v_med3_f32 v0, v197, s53, v204
	v_med3_f32 v196, v200, s53, v204
	v_cvt_pk_fp8_f32 v230, v0, v196 op_sel:[0,0,1]
	v_mul_f32_e32 v0, 0x42800000, v226
	v_mul_f32_e32 v196, 0x42800000, v227
	v_med3_f32 v0, v0, s53, v204
	v_med3_f32 v196, v196, s53, v204
	v_mov_b32_e32 v231, v1
	v_cvt_pk_fp8_f32 v231, v0, v196
	v_mul_f32_e32 v197, 0x42800000, v228
	v_mul_f32_e32 v200, 0x42800000, v229
	v_med3_f32 v0, v197, s53, v204
	v_med3_f32 v196, v200, s53, v204
	v_cvt_pk_fp8_f32 v231, v0, v196 op_sel:[0,0,1]
	v_mul_f32_e32 v0, 0x42800000, v222
	v_mul_f32_e32 v196, 0x42800000, v223
	v_med3_f32 v0, v0, s53, v204
	v_med3_f32 v196, v196, s53, v204
	v_mov_b32_e32 v232, v1
	v_cvt_pk_fp8_f32 v232, v0, v196
	v_mul_f32_e32 v197, 0x42800000, v224
	v_mul_f32_e32 v200, 0x42800000, v225
	v_med3_f32 v0, v197, s53, v204
	v_med3_f32 v196, v200, s53, v204
	v_cvt_pk_fp8_f32 v232, v0, v196 op_sel:[0,0,1]
	v_mul_f32_e32 v0, 0x42800000, v218
	v_mul_f32_e32 v196, 0x42800000, v219
	v_med3_f32 v0, v0, s53, v204
	v_med3_f32 v196, v196, s53, v204
	v_mov_b32_e32 v233, v1
	v_cvt_pk_fp8_f32 v233, v0, v196
	v_mul_f32_e32 v197, 0x42800000, v220
	v_mul_f32_e32 v200, 0x42800000, v221
	v_med3_f32 v0, v197, s53, v204
	v_med3_f32 v196, v200, s53, v204
	s_lshl_b64 s[10:11], s[58:59], 4
	v_cvt_pk_fp8_f32 v233, v0, v196 op_sel:[0,0,1]
	v_lshl_add_u64 v[196:197], v[198:199], 0, s[10:11]
	v_mul_f32_e32 v0, 0x42800000, v214
	v_mul_f32_e32 v198, 0x42800000, v215
	v_med3_f32 v0, v0, s53, v204
	v_med3_f32 v198, v198, s53, v204
	v_mov_b32_e32 v214, v1
	v_cvt_pk_fp8_f32 v214, v0, v198
	v_mul_f32_e32 v199, 0x42800000, v216
	v_mul_f32_e32 v200, 0x42800000, v217
	v_med3_f32 v0, v199, s53, v204
	v_med3_f32 v198, v200, s53, v204
	v_cvt_pk_fp8_f32 v214, v0, v198 op_sel:[0,0,1]
	v_mul_f32_e32 v0, 0x42800000, v192
	v_mul_f32_e32 v192, 0x42800000, v193
	v_med3_f32 v0, v0, s53, v204
	v_med3_f32 v192, v192, s53, v204
	v_mov_b32_e32 v215, v1
	v_cvt_pk_fp8_f32 v215, v0, v192
	v_mul_f32_e32 v193, 0x42800000, v194
	v_mul_f32_e32 v194, 0x42800000, v195
	v_med3_f32 v0, v193, s53, v204
	v_med3_f32 v192, v194, s53, v204
	v_cvt_pk_fp8_f32 v215, v0, v192 op_sel:[0,0,1]
	v_mul_f32_e32 v0, 0x42800000, v86
	v_mul_f32_e32 v86, 0x42800000, v87
	v_med3_f32 v0, v0, s53, v204
	v_med3_f32 v86, v86, s53, v204
	v_mov_b32_e32 v216, v1
	v_cvt_pk_fp8_f32 v216, v0, v86
	v_mul_f32_e32 v87, 0x42800000, v88
	v_mul_f32_e32 v88, 0x42800000, v89
	v_med3_f32 v0, v87, s53, v204
	v_med3_f32 v86, v88, s53, v204
	v_cvt_pk_fp8_f32 v216, v0, v86 op_sel:[0,0,1]
	v_mul_f32_e32 v0, 0x42800000, v82
	v_mul_f32_e32 v82, 0x42800000, v83
	v_med3_f32 v0, v0, s53, v204
	v_med3_f32 v82, v82, s53, v204
	v_mov_b32_e32 v217, v1
	v_cvt_pk_fp8_f32 v217, v0, v82
	v_mul_f32_e32 v83, 0x42800000, v84
	v_mul_f32_e32 v84, 0x42800000, v85
	v_med3_f32 v0, v83, s53, v204
	v_med3_f32 v82, v84, s53, v204
	v_cvt_pk_fp8_f32 v217, v0, v82 op_sel:[0,0,1]
	v_mul_f32_e32 v0, 0x42800000, v78
	v_mul_f32_e32 v78, 0x42800000, v79
	v_mul_f32_e32 v79, 0x42800000, v80
	v_mul_f32_e32 v80, 0x42800000, v81
	v_med3_f32 v0, v0, s53, v204
	v_med3_f32 v81, v78, s53, v204
	v_mov_b32_e32 v78, v1
	v_cvt_pk_fp8_f32 v78, v0, v81
	v_med3_f32 v0, v79, s53, v204
	v_med3_f32 v79, v80, s53, v204
	v_mov_b32_e32 v80, v1
	v_cvt_pk_fp8_f32 v78, v0, v79 op_sel:[0,0,1]
	v_mul_f32_e32 v0, 0x42800000, v74
	v_mul_f32_e32 v74, 0x42800000, v75
	v_med3_f32 v0, v0, s53, v204
	v_med3_f32 v74, v74, s53, v204
	v_mov_b32_e32 v79, v1
	v_cvt_pk_fp8_f32 v79, v0, v74
	v_mul_f32_e32 v75, 0x42800000, v76
	v_mul_f32_e32 v76, 0x42800000, v77
	v_med3_f32 v0, v75, s53, v204
	v_med3_f32 v74, v76, s53, v204
	v_cvt_pk_fp8_f32 v79, v0, v74 op_sel:[0,0,1]
	v_mul_f32_e32 v0, 0x42800000, v70
	v_mul_f32_e32 v70, 0x42800000, v71
	v_med3_f32 v0, v0, s53, v204
	v_med3_f32 v70, v70, s53, v204
	v_cvt_pk_fp8_f32 v80, v0, v70
	v_mul_f32_e32 v71, 0x42800000, v72
	v_mul_f32_e32 v72, 0x42800000, v73
	v_med3_f32 v0, v71, s53, v204
	v_med3_f32 v70, v72, s53, v204
	v_cvt_pk_fp8_f32 v80, v0, v70 op_sel:[0,0,1]
	v_mul_f32_e32 v0, 0x42800000, v66
	v_mul_f32_e32 v66, 0x42800000, v67
	v_med3_f32 v0, v0, s53, v204
	v_med3_f32 v66, v66, s53, v204
	v_mov_b32_e32 v81, v1
	v_cvt_pk_fp8_f32 v81, v0, v66
	v_mul_f32_e32 v67, 0x42800000, v68
	v_mul_f32_e32 v68, 0x42800000, v69
	v_med3_f32 v0, v67, s53, v204
	v_med3_f32 v66, v68, s53, v204
	v_cvt_pk_fp8_f32 v81, v0, v66 op_sel:[0,0,1]
	v_lshl_add_u64 v[82:83], v[196:197], 0, s[10:11]
	v_lshl_add_u64 v[66:67], v[82:83], 0, s[10:11]
	global_store_dwordx4 v[196:197], v[230:233], off nt
	global_store_dwordx4 v[82:83], v[214:217], off nt
	global_store_dwordx4 v[66:67], v[78:81], off nt
	s_waitcnt lgkmcnt(0)
	s_branch .LBB0_677
